# v14: v13 + down-GEMM epilogue row gates prefetched one tile ahead (no exposed load latency in the epilogue)
# speedup vs baseline: 1.0030x; 1.0015x over previous
; #define PG8_STAGE(bufoff, gbase, voff) do { _Pragma("unroll") for (int _i = 0; _i < 2; ++_i) \
;         __builtin_amdgcn_global_load_lds((const unsigned*)((const char*)(gbase) + (voff)[_i]), (LAS unsigned*)(lds + (bufoff) + ldsw + _i * 8192), 16, 0, 0); } while (0)
; #define PG8_WAIT_V(n) asm volatile("s_waitcnt vmcnt(" #n ")" ::: "memory")
; #define PG8_BAR __builtin_amdgcn_s_barrier()
; template <class Epi, class Sched, bool GATHER = false>
; __device__ __forceinline__ void gemm_phase(LAS unsigned char* lds, const int lda, const int ldb, const int K, const Sched& S, const Epi& E, const int* gidx = nullptr) {
;     ...
;     PG8_STAGE(PG8_SB(0, 0), cB, voffB); PG8_STAGE(PG8_SB(0, 1), cB + hstepB, voffB); PG8_STAGE(PG8_SA(0, 0), cA, ofc[0]); PG8_STAGE(PG8_SA(0, 1), cA, ofc[1]);
;     if (wr == 1) PG8_BAR;
;     PG8_WAIT_V(2); PG8_BAR;
;     PG8_STAGE(PG8_SB(1, 0), cB + kstep, voffB); PG8_STAGE(PG8_SA(1, 0), cA + kstep, ofc[0]); PG8_STAGE(PG8_SB(1, 1), cB + hstepB + kstep, voffB);
;     PG8_WAIT_V(6); PG8_BAR;
;     __device__ __forceinline__ void operator()(const AccT& acc, const GUnit& u, int wr, int wc, int fr, int fq) const {
;         float g8[2][4];
; #pragma unroll
;         for (int ai = 0; ai < 2; ++ai)
; #pragma unroll
;             for (int m = 0; m < 4; ++m) g8[ai][m] = gate[u.pm * 256 + ai * 128 + wr * 64 + m * 16 + fr];
.LBB0_1727:
	v_readlane_b32 s44, v254, 35
	s_add_u32 s28, s12, 0x40080
	v_mov_b32_e32 v135, v195
	v_readlane_b32 s45, v254, 36
	s_addc_u32 s29, s13, 0
	s_add_i32 m0, s10, 0x18000
	v_lshl_add_u64 v[2:3], v[2:3], 0, s[64:65]
	v_lshl_add_u64 v[14:15], s[44:45], 0, v[134:135]
	v_mov_b32_e32 v137, v195
	s_waitcnt vmcnt(2)
	s_barrier
	global_load_lds_dwordx4 v[2:3], off
	v_lshl_add_u64 v[2:3], v[4:5], 0, s[64:65]
	s_add_i32 m0, s10, 0x1a000
	s_add_i32 s50, s10, 0x8000
	v_lshl_add_u64 v[16:17], s[44:45], 0, v[136:137]
	global_load_lds_dwordx4 v[2:3], off
	v_lshl_add_u64 v[2:3], v[14:15], 0, s[64:65]
	s_mov_b32 m0, s50
	s_add_i32 s51, s10, 0xa000
	global_load_lds_dwordx4 v[2:3], off
	v_lshl_add_u64 v[2:3], v[16:17], 0, s[64:65]
	s_mov_b32 m0, s51
	s_mov_b32 s0, 0x40000
	global_load_lds_dwordx4 v[2:3], off
	s_add_i32 m0, s10, 0x1c000
	v_lshl_add_u64 v[2:3], s[28:29], 0, v[132:133]
	global_load_lds_dwordx4 v[2:3], off
	v_lshl_add_u64 v[2:3], s[28:29], 0, v[130:131]
	s_add_i32 m0, s10, 0x1e000
	s_lshl_b32 s28, s38, 13
	global_load_lds_dwordx4 v[2:3], off
	v_lshrrev_b32_e32 v2, 1, v6
	v_and_b32_e32 v2, 24, v2
	v_and_b32_e32 v3, 15, v6
	v_lshlrev_b32_e32 v4, 1, v2
	v_lshl_or_b32 v1, s38, 6, v3
	v_lshl_or_b32 v3, v3, 6, v4
	v_lshlrev_b32_e32 v4, 2, v6
	v_and_b32_e32 v4, 32, v4
	v_bitop3_b32 v5, v3, s28, v4 bitop3:0xde
	s_lshl_b32 s28, s37, 5
	s_and_b32 s28, s28, 0x60
	s_lshl_b32 s29, s28, 7
	v_bitop3_b32 v147, v3, s29, v4 bitop3:0xde
	v_lshlrev_b32_e32 v3, 14, v7
	v_and_b32_e32 v3, 0xffff8000, v3
	v_lshl_add_u32 v3, v8, 11, v3
	v_and_b32_e32 v4, 1, v7
	v_lshl_or_b32 v3, v4, 6, v3
	v_lshlrev_b32_e32 v4, 1, v9
	v_add3_u32 v142, v3, v4, s0
	v_lshlrev_b32_e32 v3, 14, v11
	v_and_b32_e32 v3, 0xffff8000, v3
	s_waitcnt vmcnt(6)
	v_lshl_add_u32 v3, v10, 11, v3
	v_and_b32_e32 v4, 1, v11
	s_cmpk_lt_u32 s36, 0x100
	v_lshl_or_b32 v3, v4, 6, v3
	v_lshlrev_b32_e32 v4, 1, v12
	v_mov_b32_e32 v139, v195
	v_mov_b32_e32 v141, v195
	s_cselect_b64 s[36:37], -1, 0
	v_mov_b32_e32 v143, v195
	v_add3_u32 v144, v3, v4, s0
	v_mov_b32_e32 v145, v195
	s_mov_b32 s59, 0
	v_add_u32_e32 v151, 0, v5
	s_lshl_b32 s60, s28, 1
	v_lshlrev_b32_e32 v194, 1, v2
	v_readlane_b32 s68, v254, 39
	v_readlane_b32 s69, v254, 26
	s_mov_b64 s[40:41], s[12:13]
	s_mov_b64 s[38:39], s[44:45]
	s_barrier
	v_lshl_add_u32 v244, s69, 8, v1
	v_ashrrev_i32_e32 v245, 31, v244
	v_lshl_add_u64 v[244:245], v[244:245], 2, s[62:63]
	global_load_dword v236, v[244:245], off
	global_load_dword v237, v[244:245], off offset:64
	global_load_dword v238, v[244:245], off offset:128
	global_load_dword v239, v[244:245], off offset:192
	global_load_dword v240, v[244:245], off offset:512
	global_load_dword v241, v[244:245], off offset:576
	global_load_dword v242, v[244:245], off offset:640
	global_load_dword v243, v[244:245], off offset:704
	s_branch .LBB0_1730

; __device__ __forceinline__ unsigned pk2(float lo, float hi) { unsigned r; asm("v_cvt_pk_bf16_f32 %0, %1, %2" : "=v"(r) : "v"(lo), "v"(hi)); return r; }
;     __device__ __forceinline__ void operator()(const AccT& acc, const GUnit& u, int wr, int wc, int fr, int fq) const {
;         float g8[2][4];
; #pragma unroll
;         for (int ai = 0; ai < 2; ++ai)
; #pragma unroll
;             for (int m = 0; m < 4; ++m) g8[ai][m] = gate[u.pm * 256 + ai * 128 + wr * 64 + m * 16 + fr];
; #pragma unroll
;         for (int ai = 0; ai < 2; ++ai)
; #pragma unroll
;             for (int m = 0; m < 4; ++m) {
;                 const int row = u.pm * 256 + ai * 128 + wr * 64 + m * 16 + fr;
;                 const float g = g8[ai][m];
; #pragma unroll
;                 for (int bj = 0; bj < 2; ++bj) {
;                     const f32x4 v0 = acc[ai][bj][m][0] * g, v1 = acc[ai][bj][m][1] * g;
;                     u32x4 w; w.x = pk2(v0[0], v0[1]); w.y = pk2(v0[2], v0[3]); w.z = pk2(v1[0], v1[1]); w.w = pk2(v1[2], v1[3]);
;                     *(u32x4*)(EO + (size_t)row * DM + u.pn * 256 + bj * 128 + wc * 32 + 8 * fq) = w;
.LBB0_1736:
	v_lshl_add_u32 v174, s69, 8, v1
	v_ashrrev_i32_e32 v175, 31, v174
	v_lshl_add_u64 v[148:149], v[174:175], 2, s[62:63]
	v_mov_b32_e32 v176, v236
	v_or_b32_e32 v172, 16, v174
	v_ashrrev_i32_e32 v173, 31, v172
	v_lshl_add_u64 v[148:149], v[172:173], 2, s[62:63]
	v_mov_b32_e32 v170, v237
	v_or_b32_e32 v168, 32, v174
	v_ashrrev_i32_e32 v169, 31, v168
	v_lshl_add_u64 v[148:149], v[168:169], 2, s[62:63]
	v_mov_b32_e32 v166, v238
	v_or_b32_e32 v164, 48, v174
	v_ashrrev_i32_e32 v165, 31, v164
	v_lshl_add_u64 v[148:149], v[164:165], 2, s[62:63]
	v_add_u32_e32 v160, 0x80, v174
	v_mov_b32_e32 v162, v239
	v_ashrrev_i32_e32 v161, 31, v160
	v_lshl_add_u64 v[148:149], v[160:161], 2, s[62:63]
	v_mov_b32_e32 v158, v240
	v_add_u32_e32 v156, 0x90, v174
	v_ashrrev_i32_e32 v157, 31, v156
	v_lshl_add_u64 v[148:149], v[156:157], 2, s[62:63]
	v_mov_b32_e32 v154, v241
	v_add_u32_e32 v152, 0xa0, v174
	v_ashrrev_i32_e32 v153, 31, v152
	v_lshl_add_u64 v[148:149], v[152:153], 2, s[62:63]
	v_mov_b32_e32 v150, v242
	v_add_u32_e32 v148, 0xb0, v174
	v_ashrrev_i32_e32 v149, 31, v148
	v_lshl_add_u64 v[178:179], v[148:149], 2, s[62:63]
	v_mov_b32_e32 v146, v243
	s_and_b64 vcc, exec, s[42:43]
	s_cbranch_vccz .Ldn_nogate
	v_lshl_add_u32 v244, s67, 8, v1
	v_ashrrev_i32_e32 v245, 31, v244
	v_lshl_add_u64 v[244:245], v[244:245], 2, s[62:63]
	global_load_dword v236, v[244:245], off
	global_load_dword v237, v[244:245], off offset:64
	global_load_dword v238, v[244:245], off offset:128
	global_load_dword v239, v[244:245], off offset:192
	global_load_dword v240, v[244:245], off offset:512
	global_load_dword v241, v[244:245], off offset:576
	global_load_dword v242, v[244:245], off offset:640
	global_load_dword v243, v[244:245], off offset:704
.Ldn_nogate:
	s_lshl_b32 s12, s68, 8
	s_ashr_i32 s13, s12, 31
	v_lshlrev_b64 v[174:175], 12, v[174:175]
	s_lshl_b64 s[12:13], s[12:13], 1
	s_andn2_b64 vcc, exec, s[42:43]
	s_nop 0
	v_pk_mul_f32 v[126:127], v[126:127], v[176:177] op_sel_hi:[1,0]
	v_pk_mul_f32 v[178:179], v[124:125], v[176:177] op_sel_hi:[1,0]
	v_pk_mul_f32 v[124:125], v[122:123], v[176:177] op_sel_hi:[1,0]
	v_cvt_pk_bf16_f32 v122, v126, v127
	v_lshl_add_u64 v[126:127], s[46:47], 0, v[174:175]
	v_lshl_add_u64 v[126:127], v[126:127], 0, s[12:13]
	v_lshl_add_u64 v[126:127], v[126:127], 0, s[60:61]
	v_pk_mul_f32 v[128:129], v[128:129], v[176:177] op_sel_hi:[1,0]
	v_lshl_add_u64 v[126:127], v[126:127], 0, v[194:195]
	v_cvt_pk_bf16_f32 v123, v128, v129
	v_cvt_pk_bf16_f32 v124, v124, v125
	v_cvt_pk_bf16_f32 v125, v178, v179
	global_store_dwordx4 v[126:127], v[122:125], off
	v_pk_mul_f32 v[120:121], v[120:121], v[176:177] op_sel_hi:[1,0]
	v_pk_mul_f32 v[118:119], v[118:119], v[176:177] op_sel_hi:[1,0]
	v_pk_mul_f32 v[122:123], v[116:117], v[176:177] op_sel_hi:[1,0]
	v_pk_mul_f32 v[116:117], v[114:115], v[176:177] op_sel_hi:[1,0]
	v_cvt_pk_bf16_f32 v114, v118, v119
	v_cvt_pk_bf16_f32 v115, v120, v121
	v_pk_mul_f32 v[110:111], v[110:111], v[170:171] op_sel_hi:[1,0]
	v_cvt_pk_bf16_f32 v116, v116, v117
	v_cvt_pk_bf16_f32 v117, v122, v123
	global_store_dwordx4 v[126:127], v[114:117], off offset:256
	v_pk_mul_f32 v[112:113], v[112:113], v[170:171] op_sel_hi:[1,0]
	v_pk_mul_f32 v[104:105], v[104:105], v[170:171] op_sel_hi:[1,0]
	v_lshlrev_b64 v[114:115], 12, v[172:173]
	v_pk_mul_f32 v[116:117], v[108:109], v[170:171] op_sel_hi:[1,0]
	v_pk_mul_f32 v[108:109], v[106:107], v[170:171] op_sel_hi:[1,0]
	v_cvt_pk_bf16_f32 v106, v110, v111
	v_lshl_add_u64 v[110:111], s[46:47], 0, v[114:115]
	v_lshl_add_u64 v[110:111], v[110:111], 0, s[12:13]
	v_lshl_add_u64 v[110:111], v[110:111], 0, s[60:61]
	v_cvt_pk_bf16_f32 v107, v112, v113
	v_lshl_add_u64 v[110:111], v[110:111], 0, v[194:195]
	v_cvt_pk_bf16_f32 v108, v108, v109
	v_cvt_pk_bf16_f32 v109, v116, v117
	global_store_dwordx4 v[110:111], v[106:109], off
	v_pk_mul_f32 v[102:103], v[102:103], v[170:171] op_sel_hi:[1,0]
	v_pk_mul_f32 v[94:95], v[94:95], v[166:167] op_sel_hi:[1,0]
	v_pk_mul_f32 v[106:107], v[100:101], v[170:171] op_sel_hi:[1,0]
	v_pk_mul_f32 v[100:101], v[98:99], v[170:171] op_sel_hi:[1,0]
	v_cvt_pk_bf16_f32 v98, v102, v103
	v_cvt_pk_bf16_f32 v99, v104, v105
	v_pk_mul_f32 v[96:97], v[96:97], v[166:167] op_sel_hi:[1,0]
	v_cvt_pk_bf16_f32 v100, v100, v101
	v_cvt_pk_bf16_f32 v101, v106, v107
	global_store_dwordx4 v[110:111], v[98:101], off offset:256
	v_pk_mul_f32 v[88:89], v[88:89], v[166:167] op_sel_hi:[1,0]
	v_pk_mul_f32 v[86:87], v[86:87], v[166:167] op_sel_hi:[1,0]
	v_lshlrev_b64 v[98:99], 12, v[168:169]
	v_pk_mul_f32 v[100:101], v[92:93], v[166:167] op_sel_hi:[1,0]
	v_pk_mul_f32 v[92:93], v[90:91], v[166:167] op_sel_hi:[1,0]
	v_cvt_pk_bf16_f32 v90, v94, v95
	v_lshl_add_u64 v[94:95], s[46:47], 0, v[98:99]
	v_lshl_add_u64 v[94:95], v[94:95], 0, s[12:13]
	v_lshl_add_u64 v[94:95], v[94:95], 0, s[60:61]
	v_cvt_pk_bf16_f32 v91, v96, v97
	v_lshl_add_u64 v[94:95], v[94:95], 0, v[194:195]
	v_cvt_pk_bf16_f32 v92, v92, v93
	v_cvt_pk_bf16_f32 v93, v100, v101
	global_store_dwordx4 v[94:95], v[90:93], off
	v_pk_mul_f32 v[82:83], v[82:83], v[162:163] op_sel_hi:[1,0]
	v_pk_mul_f32 v[64:65], v[64:65], v[162:163] op_sel_hi:[1,0]
	v_pk_mul_f32 v[90:91], v[80:81], v[166:167] op_sel_hi:[1,0]
	v_pk_mul_f32 v[80:81], v[78:79], v[166:167] op_sel_hi:[1,0]
	v_cvt_pk_bf16_f32 v78, v86, v87
	v_cvt_pk_bf16_f32 v79, v88, v89
	v_pk_mul_f32 v[62:63], v[62:63], v[162:163] op_sel_hi:[1,0]
	v_cvt_pk_bf16_f32 v80, v80, v81
	v_cvt_pk_bf16_f32 v81, v90, v91
; __device__ __forceinline__ unsigned pk2(float lo, float hi) { unsigned r; asm("v_cvt_pk_bf16_f32 %0, %1, %2" : "=v"(r) : "v"(lo), "v"(hi)); return r; }
; #define PG8_BAR __builtin_amdgcn_s_barrier()
; template <class Epi, class Sched, bool GATHER = false>
; __device__ __forceinline__ void gemm_phase(LAS unsigned char* lds, const int lda, const int ldb, const int K, const Sched& S, const Epi& E, const int* gidx = nullptr) {
;     ...
;         if (!has_next) break;
; #pragma unroll
;         for (int a = 0; a < 2; ++a)
; #pragma unroll
;             for (int b = 0; b < 2; ++b)
; #pragma unroll
;                 for (int m = 0; m < 4; ++m)
; #pragma unroll
;                     for (int n = 0; n < 2; ++n) acc[a][b][m][n] = (f32x4){0.f, 0.f, 0.f, 0.f};
;         cur = nxt; cA = nA; cB = nB; ++ui;
;         if constexpr (GATHER) {
; #pragma unroll
;             for (int hh = 0; hh < 2; ++hh)
; #pragma unroll
;                 for (int i = 0; i < 2; ++i) ofc[hh][i] = ofn[hh][i];
;         }
;         if (wr == 1) PG8_BAR;
;     __device__ __forceinline__ void operator()(const AccT& acc, const GUnit& u, int wr, int wc, int fr, int fq) const {
;     ...
;         for (int ai = 0; ai < 2; ++ai)
; #pragma unroll
;             for (int m = 0; m < 4; ++m) {
;                 const int row = u.pm * 256 + ai * 128 + wr * 64 + m * 16 + fr;
;                 const float g = g8[ai][m];
; #pragma unroll
;                 for (int bj = 0; bj < 2; ++bj) {
;                     const f32x4 v0 = acc[ai][bj][m][0] * g, v1 = acc[ai][bj][m][1] * g;
;                     u32x4 w; w.x = pk2(v0[0], v0[1]); w.y = pk2(v0[2], v0[3]); w.z = pk2(v1[0], v1[1]); w.w = pk2(v1[2], v1[3]);
;                     *(u32x4*)(EO + (size_t)row * DM + u.pn * 256 + bj * 128 + wc * 32 + 8 * fq) = w;
;                 }
;             }
	global_store_dwordx4 v[94:95], v[78:81], off offset:256
	v_pk_mul_f32 v[54:55], v[54:55], v[158:159] op_sel_hi:[1,0]
	v_pk_mul_f32 v[56:57], v[56:57], v[158:159] op_sel_hi:[1,0]
	v_lshlrev_b64 v[78:79], 12, v[164:165]
	v_lshl_add_u64 v[78:79], s[46:47], 0, v[78:79]
	v_lshl_add_u64 v[78:79], v[78:79], 0, s[12:13]
	v_lshl_add_u64 v[78:79], v[78:79], 0, s[60:61]
	v_pk_mul_f32 v[80:81], v[84:85], v[162:163] op_sel_hi:[1,0]
	v_pk_mul_f32 v[84:85], v[76:77], v[162:163] op_sel_hi:[1,0]
	v_pk_mul_f32 v[76:77], v[74:75], v[162:163] op_sel_hi:[1,0]
	v_cvt_pk_bf16_f32 v74, v82, v83
	v_cvt_pk_bf16_f32 v75, v80, v81
	v_lshl_add_u64 v[78:79], v[78:79], 0, v[194:195]
	v_cvt_pk_bf16_f32 v76, v76, v77
	v_cvt_pk_bf16_f32 v77, v84, v85
	global_store_dwordx4 v[78:79], v[74:77], off
	v_pk_mul_f32 v[30:31], v[30:31], v[154:155] op_sel_hi:[1,0]
	v_pk_mul_f32 v[32:33], v[32:33], v[154:155] op_sel_hi:[1,0]
	v_pk_mul_f32 v[74:75], v[60:61], v[162:163] op_sel_hi:[1,0]
	v_pk_mul_f32 v[60:61], v[58:59], v[162:163] op_sel_hi:[1,0]
	v_cvt_pk_bf16_f32 v58, v62, v63
	v_cvt_pk_bf16_f32 v59, v64, v65
	v_pk_mul_f32 v[14:15], v[14:15], v[150:151] op_sel_hi:[1,0]
	v_cvt_pk_bf16_f32 v60, v60, v61
	v_cvt_pk_bf16_f32 v61, v74, v75
	global_store_dwordx4 v[78:79], v[58:61], off offset:256
	v_pk_mul_f32 v[16:17], v[16:17], v[150:151] op_sel_hi:[1,0]
	v_pk_mul_f32 v[6:7], v[6:7], v[146:147] op_sel_hi:[1,0]
	v_lshlrev_b64 v[58:59], 12, v[160:161]
	v_pk_mul_f32 v[60:61], v[52:53], v[158:159] op_sel_hi:[1,0]
	v_pk_mul_f32 v[52:53], v[50:51], v[158:159] op_sel_hi:[1,0]
	v_cvt_pk_bf16_f32 v50, v54, v55
	v_lshl_add_u64 v[54:55], s[46:47], 0, v[58:59]
	v_lshl_add_u64 v[54:55], v[54:55], 0, s[12:13]
	v_lshl_add_u64 v[54:55], v[54:55], 0, s[60:61]
	v_cvt_pk_bf16_f32 v51, v56, v57
	v_lshl_add_u64 v[54:55], v[54:55], 0, v[194:195]
	v_cvt_pk_bf16_f32 v52, v52, v53
	v_cvt_pk_bf16_f32 v53, v60, v61
	global_store_dwordx4 v[54:55], v[50:53], off
	v_pk_mul_f32 v[56:57], v[72:73], v[158:159] op_sel_hi:[1,0]
	v_pk_mul_f32 v[58:59], v[70:71], v[158:159] op_sel_hi:[1,0]
	v_pk_mul_f32 v[50:51], v[66:67], v[158:159] op_sel_hi:[1,0]
	v_pk_mul_f32 v[52:53], v[68:69], v[158:159] op_sel_hi:[1,0]
	v_cvt_pk_bf16_f32 v50, v50, v51
	v_pk_mul_f32 v[8:9], v[8:9], v[146:147] op_sel_hi:[1,0]
	v_cvt_pk_bf16_f32 v51, v52, v53
	v_cvt_pk_bf16_f32 v52, v58, v59
	v_cvt_pk_bf16_f32 v53, v56, v57
	global_store_dwordx4 v[54:55], v[50:53], off offset:256
	s_nop 1
	v_lshlrev_b64 v[50:51], 12, v[156:157]
	v_pk_mul_f32 v[52:53], v[28:29], v[154:155] op_sel_hi:[1,0]
	v_pk_mul_f32 v[28:29], v[26:27], v[154:155] op_sel_hi:[1,0]
	v_cvt_pk_bf16_f32 v26, v30, v31
	v_lshl_add_u64 v[30:31], s[46:47], 0, v[50:51]
	v_lshl_add_u64 v[30:31], v[30:31], 0, s[12:13]
	v_lshl_add_u64 v[30:31], v[30:31], 0, s[60:61]
	v_cvt_pk_bf16_f32 v27, v32, v33
	v_lshl_add_u64 v[30:31], v[30:31], 0, v[194:195]
	v_cvt_pk_bf16_f32 v28, v28, v29
	v_cvt_pk_bf16_f32 v29, v52, v53
	global_store_dwordx4 v[30:31], v[26:29], off
	v_pk_mul_f32 v[32:33], v[48:49], v[154:155] op_sel_hi:[1,0]
	s_nop 0
	v_pk_mul_f32 v[26:27], v[42:43], v[154:155] op_sel_hi:[1,0]
	v_pk_mul_f32 v[28:29], v[44:45], v[154:155] op_sel_hi:[1,0]
	v_cvt_pk_bf16_f32 v26, v26, v27
	v_pk_mul_f32 v[42:43], v[46:47], v[154:155] op_sel_hi:[1,0]
	v_cvt_pk_bf16_f32 v27, v28, v29
	v_cvt_pk_bf16_f32 v29, v32, v33
	s_nop 0
	v_cvt_pk_bf16_f32 v28, v42, v43
	global_store_dwordx4 v[30:31], v[26:29], off offset:256
	s_nop 1
	v_lshlrev_b64 v[26:27], 12, v[152:153]
	v_pk_mul_f32 v[28:29], v[12:13], v[150:151] op_sel_hi:[1,0]
	v_pk_mul_f32 v[12:13], v[10:11], v[150:151] op_sel_hi:[1,0]
	v_cvt_pk_bf16_f32 v10, v14, v15
	v_lshl_add_u64 v[14:15], s[46:47], 0, v[26:27]
	v_lshl_add_u64 v[14:15], v[14:15], 0, s[12:13]
	v_lshl_add_u64 v[14:15], v[14:15], 0, s[60:61]
	v_cvt_pk_bf16_f32 v11, v16, v17
	v_lshl_add_u64 v[14:15], v[14:15], 0, v[194:195]
	v_cvt_pk_bf16_f32 v12, v12, v13
	v_cvt_pk_bf16_f32 v13, v28, v29
	global_store_dwordx4 v[14:15], v[10:13], off
	v_pk_mul_f32 v[16:17], v[40:41], v[150:151] op_sel_hi:[1,0]
	v_pk_mul_f32 v[26:27], v[38:39], v[150:151] op_sel_hi:[1,0]
	v_pk_mul_f32 v[10:11], v[34:35], v[150:151] op_sel_hi:[1,0]
	v_pk_mul_f32 v[12:13], v[36:37], v[150:151] op_sel_hi:[1,0]
	v_cvt_pk_bf16_f32 v10, v10, v11
	s_nop 0
	v_cvt_pk_bf16_f32 v11, v12, v13
	v_cvt_pk_bf16_f32 v12, v26, v27
	v_cvt_pk_bf16_f32 v13, v16, v17
	global_store_dwordx4 v[14:15], v[10:13], off offset:256
	s_nop 1
	v_lshlrev_b64 v[10:11], 12, v[148:149]
	v_pk_mul_f32 v[12:13], v[4:5], v[146:147] op_sel_hi:[1,0]
	v_pk_mul_f32 v[4:5], v[2:3], v[146:147] op_sel_hi:[1,0]
	v_cvt_pk_bf16_f32 v2, v6, v7
	v_lshl_add_u64 v[6:7], s[46:47], 0, v[10:11]
	v_lshl_add_u64 v[6:7], v[6:7], 0, s[12:13]
	v_lshl_add_u64 v[6:7], v[6:7], 0, s[60:61]
	v_cvt_pk_bf16_f32 v3, v8, v9
	v_cvt_pk_bf16_f32 v4, v4, v5
	v_cvt_pk_bf16_f32 v5, v12, v13
	v_lshl_add_u64 v[6:7], v[6:7], 0, v[194:195]
	global_store_dwordx4 v[6:7], v[2:5], off
	s_mov_b64 s[12:13], -1
	v_pk_mul_f32 v[8:9], v[24:25], v[146:147] op_sel_hi:[1,0]
	v_pk_mul_f32 v[4:5], v[20:21], v[146:147] op_sel_hi:[1,0]
	v_pk_mul_f32 v[2:3], v[18:19], v[146:147] op_sel_hi:[1,0]
	v_pk_mul_f32 v[10:11], v[22:23], v[146:147] op_sel_hi:[1,0]
	v_cvt_pk_bf16_f32 v2, v2, v3
	v_cvt_pk_bf16_f32 v3, v4, v5
	v_cvt_pk_bf16_f32 v5, v8, v9
	s_nop 0
	v_cvt_pk_bf16_f32 v4, v10, v11
	global_store_dwordx4 v[6:7], v[2:5], off offset:256
	s_cbranch_vccnz .LBB0_1729
	s_andn2_b64 vcc, exec, s[34:35]
	s_cbranch_vccnz .LBB0_1728
	s_barrier
	s_branch .LBB0_1728
